# v6: scanner chunk step rescheduled (all LDS operands requested up front, counted waits)
# baseline (speedup 1.0000x reference)
.LBB0_1734:
	s_mul_i32 s0, s69, 0x3300
	s_add_i32 s0, s74, s0
	s_add_i32 s1, s0, 0x2a00
	v_add_u32_e32 v18, s1, v185
	ds_read_b64_tr_b16 v[20:21], v18
	v_add3_u32 v18, s0, v186, v187
	ds_read2_b64 v[64:67], v18 offset1:4
	ds_read2_b64 v[68:71], v18 offset0:8 offset1:12
	v_add_u32_e32 v19, s0, v192
	ds_read_b128 v[80:83], v19 offset:8704
	v_add_u32_e32 v18, 0x800, v18
	ds_read2_b64 v[72:75], v18 offset0:32 offset1:36
	ds_read2_b64 v[76:79], v18 offset0:40 offset1:44
	v_add_u32_e32 v62, s0, v191
	v_add_u32_e32 v63, v62, v190
	ds_read_b128 v[104:107], v62 offset:12800
	ds_read_b128 v[108:111], v62 offset:12864
	ds_read_b128 v[112:115], v62 offset:12928
	ds_read_b128 v[116:119], v62 offset:12992
	ds_read_b128 v[88:91], v63 offset:4608
	ds_read_b128 v[92:95], v63 offset:5632
	ds_read_b128 v[96:99], v63 offset:6656
	ds_read_b128 v[100:103], v63 offset:7680
	ds_read_b128 v[84:87], v19 offset:9728
	v_cvt_pk_bf16_f32 v22, v2, v3
	v_cvt_pk_bf16_f32 v23, v4, v5
	v_cvt_pk_bf16_f32 v24, v10, v11
	v_cvt_pk_bf16_f32 v25, v12, v13
	v_cvt_pk_bf16_f32 v34, v6, v7
	v_cvt_pk_bf16_f32 v35, v8, v9
	v_cvt_pk_bf16_f32 v36, v14, v15
	v_cvt_pk_bf16_f32 v37, v16, v17
	s_waitcnt lgkmcnt(13)
	v_mfma_f32_16x16x32_bf16 v[26:29], v[64:67], v[22:25], 0
	s_waitcnt lgkmcnt(12)
	v_mfma_f32_16x16x32_bf16 v[26:29], v[68:71], v[34:37], v[26:29]
	s_waitcnt lgkmcnt(9)
	v_mfma_f32_16x16x32_bf16 v[38:41], v[72:75], v[22:25], 0
	v_mfma_f32_16x16x32_bf16 v[38:41], v[76:79], v[34:37], v[38:41]
	s_waitcnt lgkmcnt(5)
	v_pk_mul_f32 v[2:3], v[2:3], v[104:105]
	v_pk_mul_f32 v[4:5], v[4:5], v[106:107]
	v_pk_mul_f32 v[10:11], v[10:11], v[108:109]
	v_pk_mul_f32 v[12:13], v[12:13], v[110:111]
	v_pk_mul_f32 v[6:7], v[6:7], v[112:113]
	v_pk_mul_f32 v[8:9], v[8:9], v[114:115]
	v_pk_mul_f32 v[14:15], v[14:15], v[116:117]
	v_pk_mul_f32 v[16:17], v[16:17], v[118:119]
	v_cvt_pk_bf16_f32 v18, v26, v27
	v_cvt_pk_bf16_f32 v19, v28, v29
	s_nop 1
	v_mfma_f32_16x16x32_bf16 v[30:33], v[80:83], v[18:21], 0
	s_waitcnt lgkmcnt(0)
	s_add_i32 s76, s69, s68
	s_nop 5
	v_cvt_pk_bf16_f32 v18, v30, v31
	v_cvt_pk_bf16_f32 v19, v32, v33
	s_cmp_lt_u32 s76, 16
	s_nop 0
	v_mfma_f32_16x16x32_bf16 v[2:5], v[88:91], v[18:21], v[2:5]
	v_mfma_f32_16x16x32_bf16 v[10:13], v[92:95], v[18:21], v[10:13]
	v_mfma_f32_16x16x32_bf16 v[6:9], v[96:99], v[18:21], v[6:9]
	v_mfma_f32_16x16x32_bf16 v[14:17], v[100:103], v[18:21], v[14:17]
	v_mfma_f32_16x16x32_bf16 v[18:21], v[84:87], v[18:21], v[38:41]
	s_cbranch_scc1 .LBB0_1731
	s_nop 1
	v_and_b32_e32 v25, 1, v0
	v_lshl_or_b32 v24, s76, 4, v184
	v_add_u32_e32 v24, v24, v25
	v_add_u32_e32 v22, 0xffffff00, v24
	v_sub_u32_e32 v23, 0x40ff, v24
	v_cndmask_b32_e64 v22, v23, v22, s[28:29]
	v_add_u32_e32 v22, s70, v22
	v_ashrrev_i32_e32 v23, 31, v22
	v_lshlrev_b64 v[22:23], 12, v[22:23]
	v_lshl_add_u64 v[22:23], v[164:165], 0, v[22:23]
	v_sub_u32_e32 v27, 0, v25
	v_lshlrev_b32_e32 v26, 1, v27
	v_lshl_add_u64 v[22:23], v[22:23], 0, v[26:27]
	v_mov_b32_e32 v28, 0x2000
	v_mov_b32_e32 v29, 0xffffe000
	v_cndmask_b32_e64 v28, v29, v28, s[28:29]
	v_ashrrev_i32_e32 v29, 31, v28
	v_lshl_add_u64 v[30:31], v[22:23], 0, v[28:29]
	v_cmp_ne_u32_e32 vcc, 0, v25
	v_mov_b32_dpp v32, v18 quad_perm:[1,0,3,2] row_mask:0xf bank_mask:0xf bound_ctrl:1
	v_mov_b32_dpp v33, v19 quad_perm:[1,0,3,2] row_mask:0xf bank_mask:0xf bound_ctrl:1
	v_mov_b32_dpp v34, v20 quad_perm:[1,0,3,2] row_mask:0xf bank_mask:0xf bound_ctrl:1
	v_mov_b32_dpp v35, v21 quad_perm:[1,0,3,2] row_mask:0xf bank_mask:0xf bound_ctrl:1
	v_cndmask_b32_e32 v36, v18, v33, vcc
	v_cndmask_b32_e32 v37, v32, v19, vcc
	v_cndmask_b32_e32 v38, v20, v35, vcc
	v_cndmask_b32_e32 v39, v34, v21, vcc
	v_cvt_pk_bf16_f32 v36, v36, v37
	v_cvt_pk_bf16_f32 v38, v38, v39
	global_store_dword v[22:23], v36, off sc1
	global_store_dword v[30:31], v38, off sc1
	s_branch .LBB0_1731
